# v69 + closing barrier two MFMAs early in the bf16 K-loops (in-proj, out-proj)
# baseline (speedup 1.0000x reference)
.LBB0_286:
	s_lshl_b32 s10, s51, 19
	s_add_u32 s10, s20, s10
	s_addc_u32 s11, s21, 0
	s_and_b64 s[16:17], s[4:5], exec
	s_cselect_b32 s54, s11, s31
	s_cselect_b32 s55, s10, s30
	s_lshl_b32 s14, s50, 19
	s_add_u32 s16, s15, s14
	s_addc_u32 s17, s26, 0
	s_and_b64 s[36:37], s[4:5], exec
	s_cselect_b32 s56, s17, s23
	s_cselect_b32 s57, s16, s22
	s_add_i32 s60, 0, 0x10000
	v_add_u32_e32 v198, s60, v196
	s_add_i32 s62, 0, 0x14000
	v_add_u32_e32 v199, s62, v196
	ds_read_b128 v[160:163], v198
	ds_read_b128 v[152:155], v198 offset:1024
	ds_read_b128 v[156:159], v198 offset:2048
	ds_read_b128 v[148:151], v198 offset:3072
	ds_read_b128 v[144:147], v199
	ds_read_b128 v[136:139], v199 offset:1024
	ds_read_b128 v[140:143], v199 offset:2048
	ds_read_b128 v[132:135], v199 offset:3072
	s_add_u32 s36, s30, 0x40080
	s_addc_u32 s37, s31, 0
	s_add_i32 s58, s41, 0xc000
	v_lshl_add_u64 v[174:175], s[36:37], 0, v[168:169]
	s_mov_b32 m0, s58
	s_add_i32 s59, s41, 0xe000
	ds_read_b128 v[178:181], v197
	ds_read_b128 v[182:185], v197 offset:1024
	ds_read_b128 v[190:193], v197 offset:2048
	ds_read_b128 v[200:203], v197 offset:3072
	ds_read_b128 v[204:207], v197 offset:4096
	ds_read_b128 v[208:211], v197 offset:5120
	ds_read_b128 v[212:215], v197 offset:6144
	ds_read_b128 v[216:219], v197 offset:7168
	global_load_lds_dwordx4 v[174:175], off
	v_lshl_add_u64 v[174:175], s[36:37], 0, v[166:167]
	s_mov_b32 m0, s59
	s_nop 0
	global_load_lds_dwordx4 v[174:175], off
	s_waitcnt vmcnt(8)
	s_waitcnt lgkmcnt(0)
	s_barrier
	v_mfma_f32_16x16x32_bf16 v[128:131], v[160:163], v[178:181], 0
	s_setprio 1
	v_mfma_f32_16x16x32_bf16 v[124:127], v[156:159], v[178:181], 0
	v_mfma_f32_16x16x32_bf16 v[116:119], v[156:159], v[190:193], 0
	v_mfma_f32_16x16x32_bf16 v[120:123], v[160:163], v[190:193], 0
	v_mfma_f32_16x16x32_bf16 v[112:115], v[160:163], v[204:207], 0
	v_mfma_f32_16x16x32_bf16 v[108:111], v[156:159], v[204:207], 0
	v_mfma_f32_16x16x32_bf16 v[100:103], v[156:159], v[212:215], 0
	v_mfma_f32_16x16x32_bf16 v[104:107], v[160:163], v[212:215], 0
	s_nop 0
	v_mfma_f32_16x16x32_bf16 v[128:131], v[152:155], v[182:185], v[128:131]
	v_mfma_f32_16x16x32_bf16 v[124:127], v[148:151], v[182:185], v[124:127]
	v_mfma_f32_16x16x32_bf16 v[116:119], v[148:151], v[200:203], v[116:119]
	v_mfma_f32_16x16x32_bf16 v[120:123], v[152:155], v[200:203], v[120:123]
	v_mfma_f32_16x16x32_bf16 v[112:115], v[152:155], v[208:211], v[112:115]
	v_mfma_f32_16x16x32_bf16 v[108:111], v[148:151], v[208:211], v[108:111]
	v_mfma_f32_16x16x32_bf16 v[100:103], v[148:151], v[216:219], v[100:103]
	v_mfma_f32_16x16x32_bf16 v[104:107], v[152:155], v[216:219], v[104:107]
	s_setprio 0
	s_setprio 1
	v_mfma_f32_16x16x32_bf16 v[96:99], v[144:147], v[178:181], 0
	v_mfma_f32_16x16x32_bf16 v[92:95], v[140:143], v[178:181], 0
	v_mfma_f32_16x16x32_bf16 v[84:87], v[140:143], v[190:193], 0
	v_mfma_f32_16x16x32_bf16 v[88:91], v[144:147], v[190:193], 0
	v_mfma_f32_16x16x32_bf16 v[80:83], v[144:147], v[204:207], 0
	v_mfma_f32_16x16x32_bf16 v[76:79], v[140:143], v[204:207], 0
	v_mfma_f32_16x16x32_bf16 v[68:71], v[140:143], v[212:215], 0
	v_mfma_f32_16x16x32_bf16 v[72:75], v[144:147], v[212:215], 0
	s_nop 0
	v_mfma_f32_16x16x32_bf16 v[96:99], v[136:139], v[182:185], v[96:99]
	v_mfma_f32_16x16x32_bf16 v[92:95], v[132:135], v[182:185], v[92:95]
	v_mfma_f32_16x16x32_bf16 v[84:87], v[132:135], v[200:203], v[84:87]
	v_mfma_f32_16x16x32_bf16 v[88:91], v[136:139], v[200:203], v[88:91]
	v_mfma_f32_16x16x32_bf16 v[80:83], v[136:139], v[208:211], v[80:83]
	v_mfma_f32_16x16x32_bf16 v[76:79], v[132:135], v[208:211], v[76:79]
	s_barrier
	v_mfma_f32_16x16x32_bf16 v[68:71], v[132:135], v[216:219], v[68:71]
	v_mfma_f32_16x16x32_bf16 v[72:75], v[136:139], v[216:219], v[72:75]
	s_setprio 0
	v_lshl_add_u64 v[174:175], s[22:23], 0, v[34:35]
	s_add_i32 s60, s60, s40
	v_lshl_add_u64 v[190:191], v[174:175], 0, s[28:29]
	s_mov_b32 m0, s60
	s_add_i32 s61, s60, 0x2000
	ds_read_b128 v[178:181], v197 offset:16384
	ds_read_b128 v[182:185], v197 offset:17408
	ds_read_b128 v[200:203], v197 offset:18432
	ds_read_b128 v[204:207], v197 offset:19456
	ds_read_b128 v[208:211], v197 offset:20480
	ds_read_b128 v[212:215], v197 offset:21504
	ds_read_b128 v[216:219], v197 offset:22528
	ds_read_b128 v[222:225], v197 offset:23552
	global_load_lds_dwordx4 v[190:191], off
	v_lshl_add_u64 v[190:191], s[22:23], 0, v[164:165]
	s_add_u32 s36, s22, 0x40100
	v_lshl_add_u64 v[192:193], v[190:191], 0, s[28:29]
	s_mov_b32 m0, s61
	s_addc_u32 s37, s23, 0
	s_add_i32 s62, s62, s40
	global_load_lds_dwordx4 v[192:193], off
	v_lshl_add_u64 v[192:193], s[36:37], 0, v[34:35]
	s_mov_b32 m0, s62
	s_add_i32 s63, s62, 0x2000
	global_load_lds_dwordx4 v[192:193], off
	v_lshl_add_u64 v[192:193], s[36:37], 0, v[164:165]
	s_mov_b32 m0, s63
	s_nop 0
	global_load_lds_dwordx4 v[192:193], off
	v_lshl_add_u64 v[192:193], s[30:31], 0, v[168:169]
	v_lshl_add_u64 v[194:195], v[192:193], 0, s[28:29]
	s_mov_b32 m0, s41
	s_nop 0
	global_load_lds_dwordx4 v[194:195], off
	v_lshl_add_u64 v[194:195], s[30:31], 0, v[166:167]
	v_lshl_add_u64 v[226:227], v[194:195], 0, s[28:29]
	s_mov_b32 m0, s42
	s_nop 0
	global_load_lds_dwordx4 v[226:227], off
	s_waitcnt vmcnt(8)
	s_waitcnt lgkmcnt(0)
	s_barrier
	v_mfma_f32_16x16x32_bf16 v[64:67], v[160:163], v[178:181], 0
	s_setprio 1
	v_mfma_f32_16x16x32_bf16 v[60:63], v[156:159], v[178:181], 0
	v_mfma_f32_16x16x32_bf16 v[52:55], v[156:159], v[200:203], 0
	v_mfma_f32_16x16x32_bf16 v[56:59], v[160:163], v[200:203], 0
	v_mfma_f32_16x16x32_bf16 v[48:51], v[160:163], v[208:211], 0
	v_mfma_f32_16x16x32_bf16 v[44:47], v[156:159], v[208:211], 0
	v_mfma_f32_16x16x32_bf16 v[36:39], v[156:159], v[216:219], 0
	v_mfma_f32_16x16x32_bf16 v[40:43], v[160:163], v[216:219], 0
	s_nop 0
	v_mfma_f32_16x16x32_bf16 v[64:67], v[152:155], v[182:185], v[64:67]
	v_mfma_f32_16x16x32_bf16 v[60:63], v[148:151], v[182:185], v[60:63]
	v_mfma_f32_16x16x32_bf16 v[52:55], v[148:151], v[204:207], v[52:55]
	v_mfma_f32_16x16x32_bf16 v[56:59], v[152:155], v[204:207], v[56:59]
	v_mfma_f32_16x16x32_bf16 v[48:51], v[152:155], v[212:215], v[48:51]
	v_mfma_f32_16x16x32_bf16 v[44:47], v[148:151], v[212:215], v[44:47]
	v_mfma_f32_16x16x32_bf16 v[36:39], v[148:151], v[222:225], v[36:39]
	v_mfma_f32_16x16x32_bf16 v[40:43], v[152:155], v[222:225], v[40:43]
	s_setprio 0
	s_setprio 1
	v_mfma_f32_16x16x32_bf16 v[30:33], v[144:147], v[178:181], 0
	v_mfma_f32_16x16x32_bf16 v[26:29], v[140:143], v[178:181], 0
	v_mfma_f32_16x16x32_bf16 v[18:21], v[140:143], v[200:203], 0
	v_mfma_f32_16x16x32_bf16 v[22:25], v[144:147], v[200:203], 0
	v_mfma_f32_16x16x32_bf16 v[14:17], v[144:147], v[208:211], 0
	v_mfma_f32_16x16x32_bf16 v[10:13], v[140:143], v[208:211], 0
	v_mfma_f32_16x16x32_bf16 v[2:5], v[140:143], v[216:219], 0
	v_mfma_f32_16x16x32_bf16 v[6:9], v[144:147], v[216:219], 0
	s_nop 0
	v_mfma_f32_16x16x32_bf16 v[30:33], v[136:139], v[182:185], v[30:33]
	v_mfma_f32_16x16x32_bf16 v[26:29], v[132:135], v[182:185], v[26:29]
	v_mfma_f32_16x16x32_bf16 v[18:21], v[132:135], v[204:207], v[18:21]
	v_mfma_f32_16x16x32_bf16 v[22:25], v[136:139], v[204:207], v[22:25]
	v_mfma_f32_16x16x32_bf16 v[14:17], v[136:139], v[212:215], v[14:17]
	v_mfma_f32_16x16x32_bf16 v[10:13], v[132:135], v[212:215], v[10:13]
	s_barrier
	v_mfma_f32_16x16x32_bf16 v[2:5], v[132:135], v[222:225], v[2:5]
	v_mfma_f32_16x16x32_bf16 v[6:9], v[136:139], v[222:225], v[6:9]
	s_setprio 0
	s_add_i32 s64, 0, 0x18000
	s_add_i32 s66, 0, 0x1c000
	v_add_u32_e32 v132, s64, v196
	v_add_u32_e32 v133, s66, v196
	ds_read_b128 v[134:137], v132
	ds_read_b128 v[138:141], v132 offset:1024
	ds_read_b128 v[142:145], v132 offset:2048
	ds_read_b128 v[146:149], v132 offset:3072
	ds_read_b128 v[150:153], v133
	ds_read_b128 v[154:157], v133 offset:1024
	ds_read_b128 v[158:161], v133 offset:2048
	ds_read_b128 v[178:181], v133 offset:3072
	s_add_u32 s36, s30, 0x40100
	s_addc_u32 s37, s31, 0
	s_mov_b32 m0, s43
	v_lshl_add_u64 v[162:163], s[36:37], 0, v[168:169]
	ds_read_b128 v[182:185], v197 offset:32768
	ds_read_b128 v[200:203], v197 offset:33792
	ds_read_b128 v[204:207], v197 offset:34816
	ds_read_b128 v[208:211], v197 offset:35840
	ds_read_b128 v[212:215], v197 offset:36864
	ds_read_b128 v[216:219], v197 offset:37888
	ds_read_b128 v[222:225], v197 offset:38912
	ds_read_b128 v[226:229], v197 offset:39936
	global_load_lds_dwordx4 v[162:163], off
	v_lshl_add_u64 v[162:163], s[36:37], 0, v[166:167]
	s_mov_b32 m0, s44
	s_nop 0
	global_load_lds_dwordx4 v[162:163], off
	s_waitcnt vmcnt(8)
	s_waitcnt lgkmcnt(0)
	s_barrier
	v_mfma_f32_16x16x32_bf16 v[128:131], v[134:137], v[182:185], v[128:131]
	s_setprio 1
	v_mfma_f32_16x16x32_bf16 v[124:127], v[142:145], v[182:185], v[124:127]
	v_mfma_f32_16x16x32_bf16 v[116:119], v[142:145], v[204:207], v[116:119]
	v_mfma_f32_16x16x32_bf16 v[120:123], v[134:137], v[204:207], v[120:123]
	v_mfma_f32_16x16x32_bf16 v[112:115], v[134:137], v[212:215], v[112:115]
	v_mfma_f32_16x16x32_bf16 v[108:111], v[142:145], v[212:215], v[108:111]
	v_mfma_f32_16x16x32_bf16 v[100:103], v[142:145], v[222:225], v[100:103]
	v_mfma_f32_16x16x32_bf16 v[104:107], v[134:137], v[222:225], v[104:107]
	v_mfma_f32_16x16x32_bf16 v[128:131], v[138:141], v[200:203], v[128:131]
	v_mfma_f32_16x16x32_bf16 v[124:127], v[146:149], v[200:203], v[124:127]
	v_mfma_f32_16x16x32_bf16 v[116:119], v[146:149], v[208:211], v[116:119]
	v_mfma_f32_16x16x32_bf16 v[120:123], v[138:141], v[208:211], v[120:123]
	v_mfma_f32_16x16x32_bf16 v[112:115], v[138:141], v[216:219], v[112:115]
	v_mfma_f32_16x16x32_bf16 v[108:111], v[146:149], v[216:219], v[108:111]
	v_mfma_f32_16x16x32_bf16 v[100:103], v[146:149], v[226:229], v[100:103]
	v_mfma_f32_16x16x32_bf16 v[104:107], v[138:141], v[226:229], v[104:107]
	s_setprio 0
	s_setprio 1
	v_mfma_f32_16x16x32_bf16 v[96:99], v[150:153], v[182:185], v[96:99]
	v_mfma_f32_16x16x32_bf16 v[92:95], v[158:161], v[182:185], v[92:95]
	v_mfma_f32_16x16x32_bf16 v[84:87], v[158:161], v[204:207], v[84:87]
	v_mfma_f32_16x16x32_bf16 v[88:91], v[150:153], v[204:207], v[88:91]
	v_mfma_f32_16x16x32_bf16 v[80:83], v[150:153], v[212:215], v[80:83]
	v_mfma_f32_16x16x32_bf16 v[76:79], v[158:161], v[212:215], v[76:79]
	v_mfma_f32_16x16x32_bf16 v[68:71], v[158:161], v[222:225], v[68:71]
	v_mfma_f32_16x16x32_bf16 v[72:75], v[150:153], v[222:225], v[72:75]
	v_mfma_f32_16x16x32_bf16 v[96:99], v[154:157], v[200:203], v[96:99]
	v_mfma_f32_16x16x32_bf16 v[92:95], v[178:181], v[200:203], v[92:95]
	v_mfma_f32_16x16x32_bf16 v[84:87], v[178:181], v[208:211], v[84:87]
	v_mfma_f32_16x16x32_bf16 v[88:91], v[154:157], v[208:211], v[88:91]
	v_mfma_f32_16x16x32_bf16 v[80:83], v[154:157], v[216:219], v[80:83]
	v_mfma_f32_16x16x32_bf16 v[76:79], v[178:181], v[216:219], v[76:79]
	s_barrier
	v_mfma_f32_16x16x32_bf16 v[68:71], v[178:181], v[226:229], v[68:71]
	v_mfma_f32_16x16x32_bf16 v[72:75], v[154:157], v[226:229], v[72:75]
	s_setprio 0
	s_add_i32 s64, s64, s40
	s_mov_b64 s[24:25], 0x180
	s_add_i32 s65, s64, 0x2000
	v_lshl_add_u64 v[162:163], v[174:175], 0, s[24:25]
	s_mov_b32 m0, s64
	s_add_u32 s36, s22, 0x40180
	ds_read_b128 v[182:185], v197 offset:49152
	ds_read_b128 v[200:203], v197 offset:50176
	ds_read_b128 v[204:207], v197 offset:51200
	ds_read_b128 v[208:211], v197 offset:52224
	ds_read_b128 v[212:215], v197 offset:53248
	ds_read_b128 v[216:219], v197 offset:54272
	ds_read_b128 v[222:225], v197 offset:55296
	ds_read_b128 v[226:229], v197 offset:56320
	global_load_lds_dwordx4 v[162:163], off
	v_lshl_add_u64 v[162:163], v[190:191], 0, s[24:25]
	s_mov_b32 m0, s65
	s_addc_u32 s37, s23, 0
	s_add_i32 s66, s66, s40
	global_load_lds_dwordx4 v[162:163], off
	v_lshl_add_u64 v[162:163], s[36:37], 0, v[34:35]
	s_mov_b32 m0, s66
	s_add_i32 s67, s66, 0x2000
	global_load_lds_dwordx4 v[162:163], off
	v_lshl_add_u64 v[162:163], s[36:37], 0, v[164:165]
	s_mov_b32 m0, s67
	s_nop 0
	global_load_lds_dwordx4 v[162:163], off
	v_lshl_add_u64 v[162:163], v[192:193], 0, s[24:25]
	s_mov_b32 m0, s47
	s_nop 0
	global_load_lds_dwordx4 v[162:163], off
	v_lshl_add_u64 v[162:163], v[194:195], 0, s[24:25]
	s_mov_b32 m0, s48
	s_nop 0
	global_load_lds_dwordx4 v[162:163], off
	s_waitcnt vmcnt(8)
	s_waitcnt lgkmcnt(0)
	s_barrier
	v_mfma_f32_16x16x32_bf16 v[64:67], v[134:137], v[182:185], v[64:67]
	s_setprio 1
	v_mfma_f32_16x16x32_bf16 v[60:63], v[142:145], v[182:185], v[60:63]
	v_mfma_f32_16x16x32_bf16 v[52:55], v[142:145], v[204:207], v[52:55]
	v_mfma_f32_16x16x32_bf16 v[56:59], v[134:137], v[204:207], v[56:59]
	v_mfma_f32_16x16x32_bf16 v[48:51], v[134:137], v[212:215], v[48:51]
	v_mfma_f32_16x16x32_bf16 v[44:47], v[142:145], v[212:215], v[44:47]
	v_mfma_f32_16x16x32_bf16 v[36:39], v[142:145], v[222:225], v[36:39]
	v_mfma_f32_16x16x32_bf16 v[40:43], v[134:137], v[222:225], v[40:43]
	v_mfma_f32_16x16x32_bf16 v[64:67], v[138:141], v[200:203], v[64:67]
	v_mfma_f32_16x16x32_bf16 v[60:63], v[146:149], v[200:203], v[60:63]
	v_mfma_f32_16x16x32_bf16 v[52:55], v[146:149], v[208:211], v[52:55]
	v_mfma_f32_16x16x32_bf16 v[56:59], v[138:141], v[208:211], v[56:59]
	v_mfma_f32_16x16x32_bf16 v[48:51], v[138:141], v[216:219], v[48:51]
	v_mfma_f32_16x16x32_bf16 v[44:47], v[146:149], v[216:219], v[44:47]
	v_mfma_f32_16x16x32_bf16 v[36:39], v[146:149], v[226:229], v[36:39]
	v_mfma_f32_16x16x32_bf16 v[40:43], v[138:141], v[226:229], v[40:43]
	s_setprio 0
	s_setprio 1
	v_mfma_f32_16x16x32_bf16 v[30:33], v[150:153], v[182:185], v[30:33]
	v_mfma_f32_16x16x32_bf16 v[26:29], v[158:161], v[182:185], v[26:29]
	v_mfma_f32_16x16x32_bf16 v[18:21], v[158:161], v[204:207], v[18:21]
	v_mfma_f32_16x16x32_bf16 v[22:25], v[150:153], v[204:207], v[22:25]
	v_mfma_f32_16x16x32_bf16 v[14:17], v[150:153], v[212:215], v[14:17]
	v_mfma_f32_16x16x32_bf16 v[10:13], v[158:161], v[212:215], v[10:13]
	v_mfma_f32_16x16x32_bf16 v[2:5], v[158:161], v[222:225], v[2:5]
	v_mfma_f32_16x16x32_bf16 v[6:9], v[150:153], v[222:225], v[6:9]
	v_mfma_f32_16x16x32_bf16 v[30:33], v[154:157], v[200:203], v[30:33]
	v_mfma_f32_16x16x32_bf16 v[26:29], v[178:181], v[200:203], v[26:29]
	v_mfma_f32_16x16x32_bf16 v[18:21], v[178:181], v[208:211], v[18:21]
	v_mfma_f32_16x16x32_bf16 v[22:25], v[154:157], v[208:211], v[22:25]
	v_mfma_f32_16x16x32_bf16 v[14:17], v[154:157], v[216:219], v[14:17]
	v_mfma_f32_16x16x32_bf16 v[10:13], v[178:181], v[216:219], v[10:13]
	s_barrier
	v_mfma_f32_16x16x32_bf16 v[2:5], v[178:181], v[226:229], v[2:5]
	v_mfma_f32_16x16x32_bf16 v[6:9], v[154:157], v[226:229], v[6:9]
	s_setprio 0
	s_add_u32 s30, s30, 0x40180
	s_addc_u32 s31, s31, 0
	s_add_u32 s68, s22, 0x200
	s_addc_u32 s69, s23, 0
	s_mov_b32 s70, 0
.LBB0_287:
	ds_read_b128 v[134:137], v198
	ds_read_b128 v[138:141], v198 offset:1024
	ds_read_b128 v[142:145], v198 offset:2048
	ds_read_b128 v[146:149], v198 offset:3072
	ds_read_b128 v[150:153], v199
	ds_read_b128 v[154:157], v199 offset:1024
	ds_read_b128 v[158:161], v199 offset:2048
	ds_read_b128 v[178:181], v199 offset:3072
	s_add_u32 s14, s30, 0xfffc0080
	s_addc_u32 s22, s31, -1
	s_cmp_eq_u32 s70, 12
	s_cselect_b32 s37, s54, s22
	s_cselect_b32 s36, s55, s14
	s_cselect_b32 s23, s56, s69
	s_cselect_b32 s22, s57, s68
	s_mov_b32 m0, s58
	v_lshl_add_u64 v[162:163], s[30:31], 0, v[170:171]
	ds_read_b128 v[182:185], v197
	ds_read_b128 v[190:193], v197 offset:1024
	ds_read_b128 v[200:203], v197 offset:2048
	ds_read_b128 v[204:207], v197 offset:3072
	ds_read_b128 v[208:211], v197 offset:4096
	ds_read_b128 v[212:215], v197 offset:5120
	ds_read_b128 v[216:219], v197 offset:6144
	ds_read_b128 v[222:225], v197 offset:7168
	global_load_lds_dwordx4 v[162:163], off
	v_lshl_add_u64 v[162:163], s[30:31], 0, v[172:173]
	s_mov_b32 m0, s59
	s_nop 0
	global_load_lds_dwordx4 v[162:163], off
	s_waitcnt vmcnt(8)
	s_waitcnt lgkmcnt(0)
	s_barrier
	v_mfma_f32_16x16x32_bf16 v[128:131], v[134:137], v[182:185], v[128:131]
	s_setprio 1
	v_mfma_f32_16x16x32_bf16 v[124:127], v[142:145], v[182:185], v[124:127]
	v_mfma_f32_16x16x32_bf16 v[116:119], v[142:145], v[200:203], v[116:119]
	v_mfma_f32_16x16x32_bf16 v[120:123], v[134:137], v[200:203], v[120:123]
	v_mfma_f32_16x16x32_bf16 v[112:115], v[134:137], v[208:211], v[112:115]
	v_mfma_f32_16x16x32_bf16 v[108:111], v[142:145], v[208:211], v[108:111]
	v_mfma_f32_16x16x32_bf16 v[100:103], v[142:145], v[216:219], v[100:103]
	v_mfma_f32_16x16x32_bf16 v[104:107], v[134:137], v[216:219], v[104:107]
	v_mfma_f32_16x16x32_bf16 v[128:131], v[138:141], v[190:193], v[128:131]
	v_mfma_f32_16x16x32_bf16 v[124:127], v[146:149], v[190:193], v[124:127]
	v_mfma_f32_16x16x32_bf16 v[116:119], v[146:149], v[204:207], v[116:119]
	v_mfma_f32_16x16x32_bf16 v[120:123], v[138:141], v[204:207], v[120:123]
	v_mfma_f32_16x16x32_bf16 v[112:115], v[138:141], v[212:215], v[112:115]
	v_mfma_f32_16x16x32_bf16 v[108:111], v[146:149], v[212:215], v[108:111]
	v_mfma_f32_16x16x32_bf16 v[100:103], v[146:149], v[222:225], v[100:103]
	v_mfma_f32_16x16x32_bf16 v[104:107], v[138:141], v[222:225], v[104:107]
	s_setprio 0
	s_setprio 1
	v_mfma_f32_16x16x32_bf16 v[96:99], v[150:153], v[182:185], v[96:99]
	v_mfma_f32_16x16x32_bf16 v[92:95], v[158:161], v[182:185], v[92:95]
	v_mfma_f32_16x16x32_bf16 v[84:87], v[158:161], v[200:203], v[84:87]
	v_mfma_f32_16x16x32_bf16 v[88:91], v[150:153], v[200:203], v[88:91]
	v_mfma_f32_16x16x32_bf16 v[80:83], v[150:153], v[208:211], v[80:83]
	v_mfma_f32_16x16x32_bf16 v[76:79], v[158:161], v[208:211], v[76:79]
	v_mfma_f32_16x16x32_bf16 v[68:71], v[158:161], v[216:219], v[68:71]
	v_mfma_f32_16x16x32_bf16 v[72:75], v[150:153], v[216:219], v[72:75]
	v_mfma_f32_16x16x32_bf16 v[96:99], v[154:157], v[190:193], v[96:99]
	v_mfma_f32_16x16x32_bf16 v[92:95], v[178:181], v[190:193], v[92:95]
	v_mfma_f32_16x16x32_bf16 v[84:87], v[178:181], v[204:207], v[84:87]
	v_mfma_f32_16x16x32_bf16 v[88:91], v[154:157], v[204:207], v[88:91]
	v_mfma_f32_16x16x32_bf16 v[80:83], v[154:157], v[212:215], v[80:83]
	v_mfma_f32_16x16x32_bf16 v[76:79], v[178:181], v[212:215], v[76:79]
	s_barrier
	v_mfma_f32_16x16x32_bf16 v[68:71], v[178:181], v[222:225], v[68:71]
	v_mfma_f32_16x16x32_bf16 v[72:75], v[154:157], v[222:225], v[72:75]
	s_setprio 0
	s_mov_b32 m0, s60
	v_lshl_add_u64 v[162:163], s[22:23], 0, v[34:35]
	s_add_u32 s72, s22, 0x40000
	ds_read_b128 v[182:185], v197 offset:16384
	ds_read_b128 v[190:193], v197 offset:17408
	ds_read_b128 v[200:203], v197 offset:18432
	ds_read_b128 v[204:207], v197 offset:19456
	ds_read_b128 v[208:211], v197 offset:20480
	ds_read_b128 v[212:215], v197 offset:21504
	ds_read_b128 v[216:219], v197 offset:22528
	ds_read_b128 v[222:225], v197 offset:23552
	global_load_lds_dwordx4 v[162:163], off
	v_lshl_add_u64 v[174:175], s[22:23], 0, v[164:165]
	s_mov_b32 m0, s61
	s_addc_u32 s73, s23, 0
	global_load_lds_dwordx4 v[174:175], off
	v_lshl_add_u64 v[194:195], s[72:73], 0, v[34:35]
	s_mov_b32 m0, s62
	v_lshl_add_u64 v[226:227], s[36:37], 0, v[166:167]
	global_load_lds_dwordx4 v[194:195], off
	v_lshl_add_u64 v[194:195], s[72:73], 0, v[164:165]
	s_mov_b32 m0, s63
	s_nop 0
	global_load_lds_dwordx4 v[194:195], off
	v_lshl_add_u64 v[194:195], s[36:37], 0, v[168:169]
	s_mov_b32 m0, s41
	s_nop 0
	global_load_lds_dwordx4 v[194:195], off
	s_mov_b32 m0, s42
	s_nop 0
	global_load_lds_dwordx4 v[226:227], off
	s_waitcnt vmcnt(8)
	s_waitcnt lgkmcnt(0)
	s_barrier
	v_mfma_f32_16x16x32_bf16 v[64:67], v[134:137], v[182:185], v[64:67]
	s_setprio 1
	v_mfma_f32_16x16x32_bf16 v[60:63], v[142:145], v[182:185], v[60:63]
	v_mfma_f32_16x16x32_bf16 v[52:55], v[142:145], v[200:203], v[52:55]
	v_mfma_f32_16x16x32_bf16 v[56:59], v[134:137], v[200:203], v[56:59]
	v_mfma_f32_16x16x32_bf16 v[48:51], v[134:137], v[208:211], v[48:51]
	v_mfma_f32_16x16x32_bf16 v[44:47], v[142:145], v[208:211], v[44:47]
	v_mfma_f32_16x16x32_bf16 v[36:39], v[142:145], v[216:219], v[36:39]
	v_mfma_f32_16x16x32_bf16 v[40:43], v[134:137], v[216:219], v[40:43]
	v_mfma_f32_16x16x32_bf16 v[64:67], v[138:141], v[190:193], v[64:67]
	v_mfma_f32_16x16x32_bf16 v[60:63], v[146:149], v[190:193], v[60:63]
	v_mfma_f32_16x16x32_bf16 v[52:55], v[146:149], v[204:207], v[52:55]
	v_mfma_f32_16x16x32_bf16 v[56:59], v[138:141], v[204:207], v[56:59]
	v_mfma_f32_16x16x32_bf16 v[48:51], v[138:141], v[212:215], v[48:51]
	v_mfma_f32_16x16x32_bf16 v[44:47], v[146:149], v[212:215], v[44:47]
	v_mfma_f32_16x16x32_bf16 v[36:39], v[146:149], v[222:225], v[36:39]
	v_mfma_f32_16x16x32_bf16 v[40:43], v[138:141], v[222:225], v[40:43]
	s_setprio 0
	s_setprio 1
	v_mfma_f32_16x16x32_bf16 v[30:33], v[150:153], v[182:185], v[30:33]
	v_mfma_f32_16x16x32_bf16 v[26:29], v[158:161], v[182:185], v[26:29]
	v_mfma_f32_16x16x32_bf16 v[18:21], v[158:161], v[200:203], v[18:21]
	v_mfma_f32_16x16x32_bf16 v[22:25], v[150:153], v[200:203], v[22:25]
	v_mfma_f32_16x16x32_bf16 v[14:17], v[150:153], v[208:211], v[14:17]
	v_mfma_f32_16x16x32_bf16 v[10:13], v[158:161], v[208:211], v[10:13]
	v_mfma_f32_16x16x32_bf16 v[2:5], v[158:161], v[216:219], v[2:5]
	v_mfma_f32_16x16x32_bf16 v[6:9], v[150:153], v[216:219], v[6:9]
	v_mfma_f32_16x16x32_bf16 v[30:33], v[154:157], v[190:193], v[30:33]
	v_mfma_f32_16x16x32_bf16 v[26:29], v[178:181], v[190:193], v[26:29]
	v_mfma_f32_16x16x32_bf16 v[18:21], v[178:181], v[204:207], v[18:21]
	v_mfma_f32_16x16x32_bf16 v[22:25], v[154:157], v[204:207], v[22:25]
	v_mfma_f32_16x16x32_bf16 v[14:17], v[154:157], v[212:215], v[14:17]
	v_mfma_f32_16x16x32_bf16 v[10:13], v[178:181], v[212:215], v[10:13]
	s_barrier
	v_mfma_f32_16x16x32_bf16 v[2:5], v[178:181], v[222:225], v[2:5]
	v_mfma_f32_16x16x32_bf16 v[6:9], v[154:157], v[222:225], v[6:9]
	s_setprio 0
	ds_read_b128 v[134:137], v132
	ds_read_b128 v[138:141], v132 offset:1024
	ds_read_b128 v[142:145], v132 offset:2048
	ds_read_b128 v[146:149], v132 offset:3072
	ds_read_b128 v[150:153], v133
	ds_read_b128 v[154:157], v133 offset:1024
	ds_read_b128 v[158:161], v133 offset:2048
	ds_read_b128 v[178:181], v133 offset:3072
	s_add_u32 s36, s36, 0x40000
	s_addc_u32 s37, s37, 0
	s_mov_b32 m0, s43
	v_lshl_add_u64 v[228:229], s[36:37], 0, v[168:169]
	ds_read_b128 v[182:185], v197 offset:32768
	ds_read_b128 v[190:193], v197 offset:33792
	ds_read_b128 v[200:203], v197 offset:34816
	ds_read_b128 v[204:207], v197 offset:35840
	ds_read_b128 v[208:211], v197 offset:36864
	ds_read_b128 v[212:215], v197 offset:37888
	ds_read_b128 v[216:219], v197 offset:38912
	ds_read_b128 v[222:225], v197 offset:39936
	global_load_lds_dwordx4 v[228:229], off
	v_lshl_add_u64 v[228:229], s[36:37], 0, v[166:167]
	s_mov_b32 m0, s44
	s_nop 0
	global_load_lds_dwordx4 v[228:229], off
	s_waitcnt vmcnt(8)
	s_waitcnt lgkmcnt(0)
	s_barrier
	v_mfma_f32_16x16x32_bf16 v[128:131], v[134:137], v[182:185], v[128:131]
	s_setprio 1
	v_mfma_f32_16x16x32_bf16 v[124:127], v[142:145], v[182:185], v[124:127]
	v_mfma_f32_16x16x32_bf16 v[116:119], v[142:145], v[200:203], v[116:119]
	v_mfma_f32_16x16x32_bf16 v[120:123], v[134:137], v[200:203], v[120:123]
	v_mfma_f32_16x16x32_bf16 v[112:115], v[134:137], v[208:211], v[112:115]
	v_mfma_f32_16x16x32_bf16 v[108:111], v[142:145], v[208:211], v[108:111]
	v_mfma_f32_16x16x32_bf16 v[100:103], v[142:145], v[216:219], v[100:103]
	v_mfma_f32_16x16x32_bf16 v[104:107], v[134:137], v[216:219], v[104:107]
	v_mfma_f32_16x16x32_bf16 v[128:131], v[138:141], v[190:193], v[128:131]
	v_mfma_f32_16x16x32_bf16 v[124:127], v[146:149], v[190:193], v[124:127]
	v_mfma_f32_16x16x32_bf16 v[116:119], v[146:149], v[204:207], v[116:119]
	v_mfma_f32_16x16x32_bf16 v[120:123], v[138:141], v[204:207], v[120:123]
	v_mfma_f32_16x16x32_bf16 v[112:115], v[138:141], v[212:215], v[112:115]
	v_mfma_f32_16x16x32_bf16 v[108:111], v[146:149], v[212:215], v[108:111]
	v_mfma_f32_16x16x32_bf16 v[100:103], v[146:149], v[222:225], v[100:103]
	v_mfma_f32_16x16x32_bf16 v[104:107], v[138:141], v[222:225], v[104:107]
	s_setprio 0
	s_setprio 1
	v_mfma_f32_16x16x32_bf16 v[96:99], v[150:153], v[182:185], v[96:99]
	v_mfma_f32_16x16x32_bf16 v[92:95], v[158:161], v[182:185], v[92:95]
	v_mfma_f32_16x16x32_bf16 v[84:87], v[158:161], v[200:203], v[84:87]
	v_mfma_f32_16x16x32_bf16 v[88:91], v[150:153], v[200:203], v[88:91]
	v_mfma_f32_16x16x32_bf16 v[80:83], v[150:153], v[208:211], v[80:83]
	v_mfma_f32_16x16x32_bf16 v[76:79], v[158:161], v[208:211], v[76:79]
	v_mfma_f32_16x16x32_bf16 v[68:71], v[158:161], v[216:219], v[68:71]
	v_mfma_f32_16x16x32_bf16 v[72:75], v[150:153], v[216:219], v[72:75]
	v_mfma_f32_16x16x32_bf16 v[96:99], v[154:157], v[190:193], v[96:99]
	v_mfma_f32_16x16x32_bf16 v[92:95], v[178:181], v[190:193], v[92:95]
	v_mfma_f32_16x16x32_bf16 v[84:87], v[178:181], v[204:207], v[84:87]
	v_mfma_f32_16x16x32_bf16 v[88:91], v[154:157], v[204:207], v[88:91]
	v_mfma_f32_16x16x32_bf16 v[80:83], v[154:157], v[212:215], v[80:83]
	v_mfma_f32_16x16x32_bf16 v[76:79], v[178:181], v[212:215], v[76:79]
	s_barrier
	v_mfma_f32_16x16x32_bf16 v[68:71], v[178:181], v[222:225], v[68:71]
	v_mfma_f32_16x16x32_bf16 v[72:75], v[154:157], v[222:225], v[72:75]
	s_setprio 0
	s_mov_b32 m0, s64
	v_lshl_add_u64 v[162:163], v[162:163], 0, s[18:19]
	s_add_u32 s22, s22, 0x40080
	ds_read_b128 v[182:185], v197 offset:49152
	ds_read_b128 v[190:193], v197 offset:50176
	ds_read_b128 v[200:203], v197 offset:51200
	ds_read_b128 v[204:207], v197 offset:52224
	ds_read_b128 v[208:211], v197 offset:53248
	ds_read_b128 v[212:215], v197 offset:54272
	ds_read_b128 v[216:219], v197 offset:55296
	ds_read_b128 v[222:225], v197 offset:56320
	global_load_lds_dwordx4 v[162:163], off
	v_lshl_add_u64 v[162:163], v[174:175], 0, s[18:19]
	s_mov_b32 m0, s65
	s_addc_u32 s23, s23, 0
	global_load_lds_dwordx4 v[162:163], off
	v_lshl_add_u64 v[162:163], s[22:23], 0, v[34:35]
	s_mov_b32 m0, s66
	s_nop 0
	global_load_lds_dwordx4 v[162:163], off
	v_lshl_add_u64 v[162:163], s[22:23], 0, v[164:165]
	s_mov_b32 m0, s67
	s_nop 0
	global_load_lds_dwordx4 v[162:163], off
	v_lshl_add_u64 v[162:163], v[194:195], 0, s[18:19]
	s_mov_b32 m0, s47
	s_nop 0
	global_load_lds_dwordx4 v[162:163], off
	v_lshl_add_u64 v[162:163], v[226:227], 0, s[18:19]
	s_mov_b32 m0, s48
	s_nop 0
	global_load_lds_dwordx4 v[162:163], off
	s_waitcnt vmcnt(8)
	s_waitcnt lgkmcnt(0)
	s_barrier
	v_mfma_f32_16x16x32_bf16 v[64:67], v[134:137], v[182:185], v[64:67]
	s_setprio 1
	v_mfma_f32_16x16x32_bf16 v[60:63], v[142:145], v[182:185], v[60:63]
	v_mfma_f32_16x16x32_bf16 v[52:55], v[142:145], v[200:203], v[52:55]
	v_mfma_f32_16x16x32_bf16 v[56:59], v[134:137], v[200:203], v[56:59]
	v_mfma_f32_16x16x32_bf16 v[48:51], v[134:137], v[208:211], v[48:51]
	v_mfma_f32_16x16x32_bf16 v[44:47], v[142:145], v[208:211], v[44:47]
	v_mfma_f32_16x16x32_bf16 v[36:39], v[142:145], v[216:219], v[36:39]
	v_mfma_f32_16x16x32_bf16 v[40:43], v[134:137], v[216:219], v[40:43]
	v_mfma_f32_16x16x32_bf16 v[64:67], v[138:141], v[190:193], v[64:67]
	v_mfma_f32_16x16x32_bf16 v[60:63], v[146:149], v[190:193], v[60:63]
	v_mfma_f32_16x16x32_bf16 v[52:55], v[146:149], v[204:207], v[52:55]
	v_mfma_f32_16x16x32_bf16 v[56:59], v[138:141], v[204:207], v[56:59]
	v_mfma_f32_16x16x32_bf16 v[48:51], v[138:141], v[212:215], v[48:51]
	v_mfma_f32_16x16x32_bf16 v[44:47], v[146:149], v[212:215], v[44:47]
	v_mfma_f32_16x16x32_bf16 v[36:39], v[146:149], v[222:225], v[36:39]
	v_mfma_f32_16x16x32_bf16 v[40:43], v[138:141], v[222:225], v[40:43]
	s_setprio 0
	s_setprio 1
	v_mfma_f32_16x16x32_bf16 v[30:33], v[150:153], v[182:185], v[30:33]
	v_mfma_f32_16x16x32_bf16 v[26:29], v[158:161], v[182:185], v[26:29]
	v_mfma_f32_16x16x32_bf16 v[18:21], v[158:161], v[200:203], v[18:21]
	v_mfma_f32_16x16x32_bf16 v[22:25], v[150:153], v[200:203], v[22:25]
	v_mfma_f32_16x16x32_bf16 v[14:17], v[150:153], v[208:211], v[14:17]
	v_mfma_f32_16x16x32_bf16 v[10:13], v[158:161], v[208:211], v[10:13]
	v_mfma_f32_16x16x32_bf16 v[2:5], v[158:161], v[216:219], v[2:5]
	v_mfma_f32_16x16x32_bf16 v[6:9], v[150:153], v[216:219], v[6:9]
	v_mfma_f32_16x16x32_bf16 v[30:33], v[154:157], v[190:193], v[30:33]
	v_mfma_f32_16x16x32_bf16 v[26:29], v[178:181], v[190:193], v[26:29]
	v_mfma_f32_16x16x32_bf16 v[18:21], v[178:181], v[204:207], v[18:21]
	v_mfma_f32_16x16x32_bf16 v[22:25], v[154:157], v[204:207], v[22:25]
	v_mfma_f32_16x16x32_bf16 v[14:17], v[154:157], v[212:215], v[14:17]
	v_mfma_f32_16x16x32_bf16 v[10:13], v[178:181], v[212:215], v[10:13]
	s_barrier
	v_mfma_f32_16x16x32_bf16 v[2:5], v[178:181], v[222:225], v[2:5]
	v_mfma_f32_16x16x32_bf16 v[6:9], v[154:157], v[222:225], v[6:9]
	s_setprio 0
	s_add_i32 s70, s70, 2
	s_add_u32 s30, s30, 0x100
	s_addc_u32 s31, s31, 0
	s_add_u32 s68, s68, 0x100
	s_addc_u32 s69, s69, 0
	s_cmp_gt_u32 s70, 13
	s_cbranch_scc0 .LBB0_287
	s_and_b64 vcc, exec, s[8:9]
	s_cbranch_vccz .LBB0_290
	s_barrier

.LBB0_540:
	s_lshl_b32 s14, s55, 19
	v_readlane_b32 s16, v253, 53
	v_readlane_b32 s17, v253, 54
	s_add_u32 s16, s16, s14
	s_addc_u32 s17, s17, 0
	s_and_b64 s[22:23], s[4:5], exec
	s_cselect_b32 s58, s17, s37
	s_cselect_b32 s59, s16, s36
	s_lshl_b32 s14, s54, 19
	s_add_u32 s22, s15, s14
	s_addc_u32 s23, s26, 0
	s_and_b64 s[40:41], s[4:5], exec
	s_cselect_b32 s60, s23, s31
	s_cselect_b32 s61, s22, s30
	s_add_i32 s64, 0, 0x10000
	v_add_u32_e32 v172, s64, v222
	s_add_i32 s66, 0, 0x14000
	v_add_u32_e32 v173, s66, v222
	ds_read_b128 v[160:163], v172
	ds_read_b128 v[152:155], v172 offset:1024
	ds_read_b128 v[156:159], v172 offset:2048
	ds_read_b128 v[148:151], v172 offset:3072
	ds_read_b128 v[144:147], v173
	ds_read_b128 v[136:139], v173 offset:1024
	ds_read_b128 v[140:143], v173 offset:2048
	ds_read_b128 v[132:135], v173 offset:3072
	s_add_u32 s40, s36, 0x40080
	s_addc_u32 s41, s37, 0
	s_add_i32 s62, s43, 0xc000
	v_lshl_add_u64 v[174:175], s[40:41], 0, v[194:195]
	s_mov_b32 m0, s62
	s_add_i32 s63, s43, 0xe000
	ds_read_b128 v[164:167], v223
	ds_read_b128 v[168:171], v223 offset:1024
	ds_read_b128 v[178:181], v223 offset:2048
	ds_read_b128 v[182:185], v223 offset:3072
	ds_read_b128 v[200:203], v223 offset:4096
	ds_read_b128 v[204:207], v223 offset:5120
	ds_read_b128 v[208:211], v223 offset:6144
	ds_read_b128 v[212:215], v223 offset:7168
	global_load_lds_dwordx4 v[174:175], off
	v_lshl_add_u64 v[174:175], s[40:41], 0, v[192:193]
	s_mov_b32 m0, s63
	s_nop 0
	global_load_lds_dwordx4 v[174:175], off
	s_waitcnt vmcnt(8)
	s_waitcnt lgkmcnt(0)
	s_barrier
	v_mfma_f32_16x16x32_bf16 v[128:131], v[160:163], v[164:167], 0
	s_setprio 1
	v_mfma_f32_16x16x32_bf16 v[124:127], v[156:159], v[164:167], 0
	v_mfma_f32_16x16x32_bf16 v[116:119], v[156:159], v[178:181], 0
	v_mfma_f32_16x16x32_bf16 v[120:123], v[160:163], v[178:181], 0
	v_mfma_f32_16x16x32_bf16 v[112:115], v[160:163], v[200:203], 0
	v_mfma_f32_16x16x32_bf16 v[108:111], v[156:159], v[200:203], 0
	v_mfma_f32_16x16x32_bf16 v[100:103], v[156:159], v[208:211], 0
	v_mfma_f32_16x16x32_bf16 v[104:107], v[160:163], v[208:211], 0
	s_nop 0
	v_mfma_f32_16x16x32_bf16 v[128:131], v[152:155], v[168:171], v[128:131]
	v_mfma_f32_16x16x32_bf16 v[124:127], v[148:151], v[168:171], v[124:127]
	v_mfma_f32_16x16x32_bf16 v[116:119], v[148:151], v[182:185], v[116:119]
	v_mfma_f32_16x16x32_bf16 v[120:123], v[152:155], v[182:185], v[120:123]
	v_mfma_f32_16x16x32_bf16 v[112:115], v[152:155], v[204:207], v[112:115]
	v_mfma_f32_16x16x32_bf16 v[108:111], v[148:151], v[204:207], v[108:111]
	v_mfma_f32_16x16x32_bf16 v[100:103], v[148:151], v[212:215], v[100:103]
	v_mfma_f32_16x16x32_bf16 v[104:107], v[152:155], v[212:215], v[104:107]
	s_setprio 0
	s_setprio 1
	v_mfma_f32_16x16x32_bf16 v[96:99], v[144:147], v[164:167], 0
	v_mfma_f32_16x16x32_bf16 v[92:95], v[140:143], v[164:167], 0
	v_mfma_f32_16x16x32_bf16 v[84:87], v[140:143], v[178:181], 0
	v_mfma_f32_16x16x32_bf16 v[88:91], v[144:147], v[178:181], 0
	v_mfma_f32_16x16x32_bf16 v[80:83], v[144:147], v[200:203], 0
	v_mfma_f32_16x16x32_bf16 v[76:79], v[140:143], v[200:203], 0
	v_mfma_f32_16x16x32_bf16 v[68:71], v[140:143], v[208:211], 0
	v_mfma_f32_16x16x32_bf16 v[72:75], v[144:147], v[208:211], 0
	s_nop 0
	v_mfma_f32_16x16x32_bf16 v[96:99], v[136:139], v[168:171], v[96:99]
	v_mfma_f32_16x16x32_bf16 v[92:95], v[132:135], v[168:171], v[92:95]
	v_mfma_f32_16x16x32_bf16 v[84:87], v[132:135], v[182:185], v[84:87]
	v_mfma_f32_16x16x32_bf16 v[88:91], v[136:139], v[182:185], v[88:91]
	v_mfma_f32_16x16x32_bf16 v[80:83], v[136:139], v[204:207], v[80:83]
	v_mfma_f32_16x16x32_bf16 v[76:79], v[132:135], v[204:207], v[76:79]
	s_barrier
	v_mfma_f32_16x16x32_bf16 v[68:71], v[132:135], v[212:215], v[68:71]
	v_mfma_f32_16x16x32_bf16 v[72:75], v[136:139], v[212:215], v[72:75]
	s_setprio 0
	v_lshl_add_u64 v[164:165], s[30:31], 0, v[34:35]
	s_add_i32 s64, s64, s42
	v_lshl_add_u64 v[166:167], v[164:165], 0, s[28:29]
	s_mov_b32 m0, s64
	s_add_i32 s65, s64, 0x2000
	ds_read_b128 v[178:181], v223 offset:16384
	ds_read_b128 v[182:185], v223 offset:17408
	ds_read_b128 v[200:203], v223 offset:18432
	ds_read_b128 v[204:207], v223 offset:19456
	ds_read_b128 v[208:211], v223 offset:20480
	ds_read_b128 v[212:215], v223 offset:21504
	ds_read_b128 v[216:219], v223 offset:22528
	ds_read_b128 v[224:227], v223 offset:23552
	global_load_lds_dwordx4 v[166:167], off
	v_lshl_add_u64 v[166:167], s[30:31], 0, v[190:191]
	s_add_u32 s40, s30, 0x40100
	v_lshl_add_u64 v[168:169], v[166:167], 0, s[28:29]
	s_mov_b32 m0, s65
	s_addc_u32 s41, s31, 0
	s_add_i32 s66, s66, s42
	global_load_lds_dwordx4 v[168:169], off
	v_lshl_add_u64 v[168:169], s[40:41], 0, v[34:35]
	s_mov_b32 m0, s66
	s_add_i32 s67, s66, 0x2000
	global_load_lds_dwordx4 v[168:169], off
	v_lshl_add_u64 v[168:169], s[40:41], 0, v[190:191]
	s_mov_b32 m0, s67
	s_nop 0
	global_load_lds_dwordx4 v[168:169], off
	v_lshl_add_u64 v[168:169], s[36:37], 0, v[194:195]
	v_lshl_add_u64 v[170:171], v[168:169], 0, s[28:29]
	s_mov_b32 m0, s43
	s_nop 0
	global_load_lds_dwordx4 v[170:171], off
	v_lshl_add_u64 v[170:171], s[36:37], 0, v[192:193]
	v_lshl_add_u64 v[174:175], v[170:171], 0, s[28:29]
	s_mov_b32 m0, s44
	s_nop 0
	global_load_lds_dwordx4 v[174:175], off
	s_waitcnt vmcnt(8)
	s_waitcnt lgkmcnt(0)
	s_barrier
	v_mfma_f32_16x16x32_bf16 v[64:67], v[160:163], v[178:181], 0
	s_setprio 1
	v_mfma_f32_16x16x32_bf16 v[60:63], v[156:159], v[178:181], 0
	v_mfma_f32_16x16x32_bf16 v[52:55], v[156:159], v[200:203], 0
	v_mfma_f32_16x16x32_bf16 v[56:59], v[160:163], v[200:203], 0
	v_mfma_f32_16x16x32_bf16 v[48:51], v[160:163], v[208:211], 0
	v_mfma_f32_16x16x32_bf16 v[44:47], v[156:159], v[208:211], 0
	v_mfma_f32_16x16x32_bf16 v[36:39], v[156:159], v[216:219], 0
	v_mfma_f32_16x16x32_bf16 v[40:43], v[160:163], v[216:219], 0
	s_nop 0
	v_mfma_f32_16x16x32_bf16 v[64:67], v[152:155], v[182:185], v[64:67]
	v_mfma_f32_16x16x32_bf16 v[60:63], v[148:151], v[182:185], v[60:63]
	v_mfma_f32_16x16x32_bf16 v[52:55], v[148:151], v[204:207], v[52:55]
	v_mfma_f32_16x16x32_bf16 v[56:59], v[152:155], v[204:207], v[56:59]
	v_mfma_f32_16x16x32_bf16 v[48:51], v[152:155], v[212:215], v[48:51]
	v_mfma_f32_16x16x32_bf16 v[44:47], v[148:151], v[212:215], v[44:47]
	v_mfma_f32_16x16x32_bf16 v[36:39], v[148:151], v[224:227], v[36:39]
	v_mfma_f32_16x16x32_bf16 v[40:43], v[152:155], v[224:227], v[40:43]
	s_setprio 0
	s_setprio 1
	v_mfma_f32_16x16x32_bf16 v[30:33], v[144:147], v[178:181], 0
	v_mfma_f32_16x16x32_bf16 v[26:29], v[140:143], v[178:181], 0
	v_mfma_f32_16x16x32_bf16 v[18:21], v[140:143], v[200:203], 0
	v_mfma_f32_16x16x32_bf16 v[22:25], v[144:147], v[200:203], 0
	v_mfma_f32_16x16x32_bf16 v[14:17], v[144:147], v[208:211], 0
	v_mfma_f32_16x16x32_bf16 v[10:13], v[140:143], v[208:211], 0
	v_mfma_f32_16x16x32_bf16 v[2:5], v[140:143], v[216:219], 0
	v_mfma_f32_16x16x32_bf16 v[6:9], v[144:147], v[216:219], 0
	s_nop 0
	v_mfma_f32_16x16x32_bf16 v[30:33], v[136:139], v[182:185], v[30:33]
	v_mfma_f32_16x16x32_bf16 v[26:29], v[132:135], v[182:185], v[26:29]
	v_mfma_f32_16x16x32_bf16 v[18:21], v[132:135], v[204:207], v[18:21]
	v_mfma_f32_16x16x32_bf16 v[22:25], v[136:139], v[204:207], v[22:25]
	v_mfma_f32_16x16x32_bf16 v[14:17], v[136:139], v[212:215], v[14:17]
	v_mfma_f32_16x16x32_bf16 v[10:13], v[132:135], v[212:215], v[10:13]
	s_barrier
	v_mfma_f32_16x16x32_bf16 v[2:5], v[132:135], v[224:227], v[2:5]
	v_mfma_f32_16x16x32_bf16 v[6:9], v[136:139], v[224:227], v[6:9]
	s_setprio 0
	s_add_i32 s68, 0, 0x18000
	s_add_i32 s70, 0, 0x1c000
	v_add_u32_e32 v132, s68, v222
	v_add_u32_e32 v133, s70, v222
	ds_read_b128 v[134:137], v132
	ds_read_b128 v[138:141], v132 offset:1024
	ds_read_b128 v[142:145], v132 offset:2048
	ds_read_b128 v[146:149], v132 offset:3072
	ds_read_b128 v[150:153], v133
	ds_read_b128 v[154:157], v133 offset:1024
	ds_read_b128 v[158:161], v133 offset:2048
	ds_read_b128 v[178:181], v133 offset:3072
	s_add_u32 s40, s36, 0x40100
	s_addc_u32 s41, s37, 0
	s_mov_b32 m0, s45
	v_lshl_add_u64 v[162:163], s[40:41], 0, v[194:195]
	ds_read_b128 v[182:185], v223 offset:32768
	ds_read_b128 v[200:203], v223 offset:33792
	ds_read_b128 v[204:207], v223 offset:34816
	ds_read_b128 v[208:211], v223 offset:35840
	ds_read_b128 v[212:215], v223 offset:36864
	ds_read_b128 v[216:219], v223 offset:37888
	ds_read_b128 v[224:227], v223 offset:38912
	ds_read_b128 v[228:231], v223 offset:39936
	global_load_lds_dwordx4 v[162:163], off
	v_lshl_add_u64 v[162:163], s[40:41], 0, v[192:193]
	s_mov_b32 m0, s46
	s_nop 0
	global_load_lds_dwordx4 v[162:163], off
	s_waitcnt vmcnt(8)
	s_waitcnt lgkmcnt(0)
	s_barrier
	v_mfma_f32_16x16x32_bf16 v[128:131], v[134:137], v[182:185], v[128:131]
	s_setprio 1
	v_mfma_f32_16x16x32_bf16 v[124:127], v[142:145], v[182:185], v[124:127]
	v_mfma_f32_16x16x32_bf16 v[116:119], v[142:145], v[204:207], v[116:119]
	v_mfma_f32_16x16x32_bf16 v[120:123], v[134:137], v[204:207], v[120:123]
	v_mfma_f32_16x16x32_bf16 v[112:115], v[134:137], v[212:215], v[112:115]
	v_mfma_f32_16x16x32_bf16 v[108:111], v[142:145], v[212:215], v[108:111]
	v_mfma_f32_16x16x32_bf16 v[100:103], v[142:145], v[224:227], v[100:103]
	v_mfma_f32_16x16x32_bf16 v[104:107], v[134:137], v[224:227], v[104:107]
	v_mfma_f32_16x16x32_bf16 v[128:131], v[138:141], v[200:203], v[128:131]
	v_mfma_f32_16x16x32_bf16 v[124:127], v[146:149], v[200:203], v[124:127]
	v_mfma_f32_16x16x32_bf16 v[116:119], v[146:149], v[208:211], v[116:119]
	v_mfma_f32_16x16x32_bf16 v[120:123], v[138:141], v[208:211], v[120:123]
	v_mfma_f32_16x16x32_bf16 v[112:115], v[138:141], v[216:219], v[112:115]
	v_mfma_f32_16x16x32_bf16 v[108:111], v[146:149], v[216:219], v[108:111]
	v_mfma_f32_16x16x32_bf16 v[100:103], v[146:149], v[228:231], v[100:103]
	v_mfma_f32_16x16x32_bf16 v[104:107], v[138:141], v[228:231], v[104:107]
	s_setprio 0
	s_setprio 1
	v_mfma_f32_16x16x32_bf16 v[96:99], v[150:153], v[182:185], v[96:99]
	v_mfma_f32_16x16x32_bf16 v[92:95], v[158:161], v[182:185], v[92:95]
	v_mfma_f32_16x16x32_bf16 v[84:87], v[158:161], v[204:207], v[84:87]
	v_mfma_f32_16x16x32_bf16 v[88:91], v[150:153], v[204:207], v[88:91]
	v_mfma_f32_16x16x32_bf16 v[80:83], v[150:153], v[212:215], v[80:83]
	v_mfma_f32_16x16x32_bf16 v[76:79], v[158:161], v[212:215], v[76:79]
	v_mfma_f32_16x16x32_bf16 v[68:71], v[158:161], v[224:227], v[68:71]
	v_mfma_f32_16x16x32_bf16 v[72:75], v[150:153], v[224:227], v[72:75]
	v_mfma_f32_16x16x32_bf16 v[96:99], v[154:157], v[200:203], v[96:99]
	v_mfma_f32_16x16x32_bf16 v[92:95], v[178:181], v[200:203], v[92:95]
	v_mfma_f32_16x16x32_bf16 v[84:87], v[178:181], v[208:211], v[84:87]
	v_mfma_f32_16x16x32_bf16 v[88:91], v[154:157], v[208:211], v[88:91]
	v_mfma_f32_16x16x32_bf16 v[80:83], v[154:157], v[216:219], v[80:83]
	v_mfma_f32_16x16x32_bf16 v[76:79], v[178:181], v[216:219], v[76:79]
	s_barrier
	v_mfma_f32_16x16x32_bf16 v[68:71], v[178:181], v[228:231], v[68:71]
	v_mfma_f32_16x16x32_bf16 v[72:75], v[154:157], v[228:231], v[72:75]
	s_setprio 0
	s_add_i32 s68, s68, s42
	s_mov_b64 s[24:25], 0x180
	s_add_i32 s69, s68, 0x2000
	v_lshl_add_u64 v[162:163], v[164:165], 0, s[24:25]
	s_mov_b32 m0, s68
	s_add_u32 s40, s30, 0x40180
	ds_read_b128 v[182:185], v223 offset:49152
	ds_read_b128 v[200:203], v223 offset:50176
	ds_read_b128 v[204:207], v223 offset:51200
	ds_read_b128 v[208:211], v223 offset:52224
	ds_read_b128 v[212:215], v223 offset:53248
	ds_read_b128 v[216:219], v223 offset:54272
	ds_read_b128 v[224:227], v223 offset:55296
	ds_read_b128 v[228:231], v223 offset:56320
	global_load_lds_dwordx4 v[162:163], off
	v_lshl_add_u64 v[162:163], v[166:167], 0, s[24:25]
	s_mov_b32 m0, s69
	s_addc_u32 s41, s31, 0
	s_add_i32 s70, s70, s42
	global_load_lds_dwordx4 v[162:163], off
	v_lshl_add_u64 v[162:163], s[40:41], 0, v[34:35]
	s_mov_b32 m0, s70
	s_add_i32 s71, s70, 0x2000
	global_load_lds_dwordx4 v[162:163], off
	v_lshl_add_u64 v[162:163], s[40:41], 0, v[190:191]
	s_mov_b32 m0, s71
	s_nop 0
	global_load_lds_dwordx4 v[162:163], off
	v_lshl_add_u64 v[162:163], v[168:169], 0, s[24:25]
	s_mov_b32 m0, s51
	s_nop 0
	global_load_lds_dwordx4 v[162:163], off
	v_lshl_add_u64 v[162:163], v[170:171], 0, s[24:25]
	s_mov_b32 m0, s52
	s_nop 0
	global_load_lds_dwordx4 v[162:163], off
	s_waitcnt vmcnt(8)
	s_waitcnt lgkmcnt(0)
	s_barrier
	v_mfma_f32_16x16x32_bf16 v[64:67], v[134:137], v[182:185], v[64:67]
	s_setprio 1
	v_mfma_f32_16x16x32_bf16 v[60:63], v[142:145], v[182:185], v[60:63]
	v_mfma_f32_16x16x32_bf16 v[52:55], v[142:145], v[204:207], v[52:55]
	v_mfma_f32_16x16x32_bf16 v[56:59], v[134:137], v[204:207], v[56:59]
	v_mfma_f32_16x16x32_bf16 v[48:51], v[134:137], v[212:215], v[48:51]
	v_mfma_f32_16x16x32_bf16 v[44:47], v[142:145], v[212:215], v[44:47]
	v_mfma_f32_16x16x32_bf16 v[36:39], v[142:145], v[224:227], v[36:39]
	v_mfma_f32_16x16x32_bf16 v[40:43], v[134:137], v[224:227], v[40:43]
	v_mfma_f32_16x16x32_bf16 v[64:67], v[138:141], v[200:203], v[64:67]
	v_mfma_f32_16x16x32_bf16 v[60:63], v[146:149], v[200:203], v[60:63]
	v_mfma_f32_16x16x32_bf16 v[52:55], v[146:149], v[208:211], v[52:55]
	v_mfma_f32_16x16x32_bf16 v[56:59], v[138:141], v[208:211], v[56:59]
	v_mfma_f32_16x16x32_bf16 v[48:51], v[138:141], v[216:219], v[48:51]
	v_mfma_f32_16x16x32_bf16 v[44:47], v[146:149], v[216:219], v[44:47]
	v_mfma_f32_16x16x32_bf16 v[36:39], v[146:149], v[228:231], v[36:39]
	v_mfma_f32_16x16x32_bf16 v[40:43], v[138:141], v[228:231], v[40:43]
	s_setprio 0
	s_setprio 1
	v_mfma_f32_16x16x32_bf16 v[30:33], v[150:153], v[182:185], v[30:33]
	v_mfma_f32_16x16x32_bf16 v[26:29], v[158:161], v[182:185], v[26:29]
	v_mfma_f32_16x16x32_bf16 v[18:21], v[158:161], v[204:207], v[18:21]
	v_mfma_f32_16x16x32_bf16 v[22:25], v[150:153], v[204:207], v[22:25]
	v_mfma_f32_16x16x32_bf16 v[14:17], v[150:153], v[212:215], v[14:17]
	v_mfma_f32_16x16x32_bf16 v[10:13], v[158:161], v[212:215], v[10:13]
	v_mfma_f32_16x16x32_bf16 v[2:5], v[158:161], v[224:227], v[2:5]
	v_mfma_f32_16x16x32_bf16 v[6:9], v[150:153], v[224:227], v[6:9]
	v_mfma_f32_16x16x32_bf16 v[30:33], v[154:157], v[200:203], v[30:33]
	v_mfma_f32_16x16x32_bf16 v[26:29], v[178:181], v[200:203], v[26:29]
	v_mfma_f32_16x16x32_bf16 v[18:21], v[178:181], v[208:211], v[18:21]
	v_mfma_f32_16x16x32_bf16 v[22:25], v[154:157], v[208:211], v[22:25]
	v_mfma_f32_16x16x32_bf16 v[14:17], v[154:157], v[216:219], v[14:17]
	v_mfma_f32_16x16x32_bf16 v[10:13], v[178:181], v[216:219], v[10:13]
	s_barrier
	v_mfma_f32_16x16x32_bf16 v[2:5], v[178:181], v[228:231], v[2:5]
	v_mfma_f32_16x16x32_bf16 v[6:9], v[154:157], v[228:231], v[6:9]
	s_setprio 0
	s_add_u32 s36, s36, 0x40180
	s_addc_u32 s37, s37, 0
	s_add_u32 s72, s30, 0x200
	s_addc_u32 s73, s31, 0
	s_mov_b32 s74, 0
.LBB0_541:
	ds_read_b128 v[134:137], v172
	ds_read_b128 v[138:141], v172 offset:1024
	ds_read_b128 v[142:145], v172 offset:2048
	ds_read_b128 v[146:149], v172 offset:3072
	ds_read_b128 v[150:153], v173
	ds_read_b128 v[154:157], v173 offset:1024
	ds_read_b128 v[158:161], v173 offset:2048
	ds_read_b128 v[162:165], v173 offset:3072
	s_add_u32 s14, s36, 0xfffc0080
	s_addc_u32 s30, s37, -1
	s_cmp_eq_u32 s74, 12
	s_cselect_b32 s41, s58, s30
	s_cselect_b32 s40, s59, s14
	s_cselect_b32 s31, s60, s73
	s_cselect_b32 s30, s61, s72
	s_mov_b32 m0, s62
	v_lshl_add_u64 v[170:171], s[36:37], 0, v[196:197]
	ds_read_b128 v[166:169], v223
	ds_read_b128 v[178:181], v223 offset:1024
	ds_read_b128 v[182:185], v223 offset:2048
	ds_read_b128 v[200:203], v223 offset:3072
	ds_read_b128 v[204:207], v223 offset:4096
	ds_read_b128 v[208:211], v223 offset:5120
	ds_read_b128 v[212:215], v223 offset:6144
	ds_read_b128 v[216:219], v223 offset:7168
	global_load_lds_dwordx4 v[170:171], off
	v_lshl_add_u64 v[170:171], s[36:37], 0, v[198:199]
	s_mov_b32 m0, s63
	s_nop 0
	global_load_lds_dwordx4 v[170:171], off
	s_waitcnt vmcnt(8)
	s_waitcnt lgkmcnt(0)
	s_barrier
	v_mfma_f32_16x16x32_bf16 v[128:131], v[134:137], v[166:169], v[128:131]
	s_setprio 1
	v_mfma_f32_16x16x32_bf16 v[124:127], v[142:145], v[166:169], v[124:127]
	v_mfma_f32_16x16x32_bf16 v[116:119], v[142:145], v[182:185], v[116:119]
	v_mfma_f32_16x16x32_bf16 v[120:123], v[134:137], v[182:185], v[120:123]
	v_mfma_f32_16x16x32_bf16 v[112:115], v[134:137], v[204:207], v[112:115]
	v_mfma_f32_16x16x32_bf16 v[108:111], v[142:145], v[204:207], v[108:111]
	v_mfma_f32_16x16x32_bf16 v[100:103], v[142:145], v[212:215], v[100:103]
	v_mfma_f32_16x16x32_bf16 v[104:107], v[134:137], v[212:215], v[104:107]
	v_mfma_f32_16x16x32_bf16 v[128:131], v[138:141], v[178:181], v[128:131]
	v_mfma_f32_16x16x32_bf16 v[124:127], v[146:149], v[178:181], v[124:127]
	v_mfma_f32_16x16x32_bf16 v[116:119], v[146:149], v[200:203], v[116:119]
	v_mfma_f32_16x16x32_bf16 v[120:123], v[138:141], v[200:203], v[120:123]
	v_mfma_f32_16x16x32_bf16 v[112:115], v[138:141], v[208:211], v[112:115]
	v_mfma_f32_16x16x32_bf16 v[108:111], v[146:149], v[208:211], v[108:111]
	v_mfma_f32_16x16x32_bf16 v[100:103], v[146:149], v[216:219], v[100:103]
	v_mfma_f32_16x16x32_bf16 v[104:107], v[138:141], v[216:219], v[104:107]
	s_setprio 0
	s_setprio 1
	v_mfma_f32_16x16x32_bf16 v[96:99], v[150:153], v[166:169], v[96:99]
	v_mfma_f32_16x16x32_bf16 v[92:95], v[158:161], v[166:169], v[92:95]
	v_mfma_f32_16x16x32_bf16 v[84:87], v[158:161], v[182:185], v[84:87]
	v_mfma_f32_16x16x32_bf16 v[88:91], v[150:153], v[182:185], v[88:91]
	v_mfma_f32_16x16x32_bf16 v[80:83], v[150:153], v[204:207], v[80:83]
	v_mfma_f32_16x16x32_bf16 v[76:79], v[158:161], v[204:207], v[76:79]
	v_mfma_f32_16x16x32_bf16 v[68:71], v[158:161], v[212:215], v[68:71]
	v_mfma_f32_16x16x32_bf16 v[72:75], v[150:153], v[212:215], v[72:75]
	v_mfma_f32_16x16x32_bf16 v[96:99], v[154:157], v[178:181], v[96:99]
	v_mfma_f32_16x16x32_bf16 v[92:95], v[162:165], v[178:181], v[92:95]
	v_mfma_f32_16x16x32_bf16 v[84:87], v[162:165], v[200:203], v[84:87]
	v_mfma_f32_16x16x32_bf16 v[88:91], v[154:157], v[200:203], v[88:91]
	v_mfma_f32_16x16x32_bf16 v[80:83], v[154:157], v[208:211], v[80:83]
	v_mfma_f32_16x16x32_bf16 v[76:79], v[162:165], v[208:211], v[76:79]
	s_barrier
	v_mfma_f32_16x16x32_bf16 v[68:71], v[162:165], v[216:219], v[68:71]
	v_mfma_f32_16x16x32_bf16 v[72:75], v[154:157], v[216:219], v[72:75]
	s_setprio 0
	s_mov_b32 m0, s64
	v_lshl_add_u64 v[170:171], s[30:31], 0, v[34:35]
	s_add_u32 s76, s30, 0x40000
	ds_read_b128 v[166:169], v223 offset:16384
	ds_read_b128 v[178:181], v223 offset:17408
	ds_read_b128 v[182:185], v223 offset:18432
	ds_read_b128 v[200:203], v223 offset:19456
	ds_read_b128 v[204:207], v223 offset:20480
	ds_read_b128 v[208:211], v223 offset:21504
	ds_read_b128 v[212:215], v223 offset:22528
	ds_read_b128 v[216:219], v223 offset:23552
	global_load_lds_dwordx4 v[170:171], off
	v_lshl_add_u64 v[174:175], s[30:31], 0, v[190:191]
	s_mov_b32 m0, s65
	s_addc_u32 s77, s31, 0
	global_load_lds_dwordx4 v[174:175], off
	v_lshl_add_u64 v[224:225], s[76:77], 0, v[34:35]
	s_mov_b32 m0, s66
	v_lshl_add_u64 v[226:227], s[40:41], 0, v[192:193]
	global_load_lds_dwordx4 v[224:225], off
	v_lshl_add_u64 v[224:225], s[76:77], 0, v[190:191]
	s_mov_b32 m0, s67
	s_nop 0
	global_load_lds_dwordx4 v[224:225], off
	v_lshl_add_u64 v[224:225], s[40:41], 0, v[194:195]
	s_mov_b32 m0, s43
	s_nop 0
	global_load_lds_dwordx4 v[224:225], off
	s_mov_b32 m0, s44
	s_nop 0
	global_load_lds_dwordx4 v[226:227], off
	s_waitcnt vmcnt(8)
	s_waitcnt lgkmcnt(0)
	s_barrier
	v_mfma_f32_16x16x32_bf16 v[64:67], v[134:137], v[166:169], v[64:67]
	s_setprio 1
	v_mfma_f32_16x16x32_bf16 v[60:63], v[142:145], v[166:169], v[60:63]
	v_mfma_f32_16x16x32_bf16 v[52:55], v[142:145], v[182:185], v[52:55]
	v_mfma_f32_16x16x32_bf16 v[56:59], v[134:137], v[182:185], v[56:59]
	v_mfma_f32_16x16x32_bf16 v[48:51], v[134:137], v[204:207], v[48:51]
	v_mfma_f32_16x16x32_bf16 v[44:47], v[142:145], v[204:207], v[44:47]
	v_mfma_f32_16x16x32_bf16 v[36:39], v[142:145], v[212:215], v[36:39]
	v_mfma_f32_16x16x32_bf16 v[40:43], v[134:137], v[212:215], v[40:43]
	v_mfma_f32_16x16x32_bf16 v[64:67], v[138:141], v[178:181], v[64:67]
	v_mfma_f32_16x16x32_bf16 v[60:63], v[146:149], v[178:181], v[60:63]
	v_mfma_f32_16x16x32_bf16 v[52:55], v[146:149], v[200:203], v[52:55]
	v_mfma_f32_16x16x32_bf16 v[56:59], v[138:141], v[200:203], v[56:59]
	v_mfma_f32_16x16x32_bf16 v[48:51], v[138:141], v[208:211], v[48:51]
	v_mfma_f32_16x16x32_bf16 v[44:47], v[146:149], v[208:211], v[44:47]
	v_mfma_f32_16x16x32_bf16 v[36:39], v[146:149], v[216:219], v[36:39]
	v_mfma_f32_16x16x32_bf16 v[40:43], v[138:141], v[216:219], v[40:43]
	s_setprio 0
	s_setprio 1
	v_mfma_f32_16x16x32_bf16 v[30:33], v[150:153], v[166:169], v[30:33]
	v_mfma_f32_16x16x32_bf16 v[26:29], v[158:161], v[166:169], v[26:29]
	v_mfma_f32_16x16x32_bf16 v[18:21], v[158:161], v[182:185], v[18:21]
	v_mfma_f32_16x16x32_bf16 v[22:25], v[150:153], v[182:185], v[22:25]
	v_mfma_f32_16x16x32_bf16 v[14:17], v[150:153], v[204:207], v[14:17]
	v_mfma_f32_16x16x32_bf16 v[10:13], v[158:161], v[204:207], v[10:13]
	v_mfma_f32_16x16x32_bf16 v[2:5], v[158:161], v[212:215], v[2:5]
	v_mfma_f32_16x16x32_bf16 v[6:9], v[150:153], v[212:215], v[6:9]
	v_mfma_f32_16x16x32_bf16 v[30:33], v[154:157], v[178:181], v[30:33]
	v_mfma_f32_16x16x32_bf16 v[26:29], v[162:165], v[178:181], v[26:29]
	v_mfma_f32_16x16x32_bf16 v[18:21], v[162:165], v[200:203], v[18:21]
	v_mfma_f32_16x16x32_bf16 v[22:25], v[154:157], v[200:203], v[22:25]
	v_mfma_f32_16x16x32_bf16 v[14:17], v[154:157], v[208:211], v[14:17]
	v_mfma_f32_16x16x32_bf16 v[10:13], v[162:165], v[208:211], v[10:13]
	s_barrier
	v_mfma_f32_16x16x32_bf16 v[2:5], v[162:165], v[216:219], v[2:5]
	v_mfma_f32_16x16x32_bf16 v[6:9], v[154:157], v[216:219], v[6:9]
	s_setprio 0
	ds_read_b128 v[134:137], v132
	ds_read_b128 v[138:141], v132 offset:1024
	ds_read_b128 v[142:145], v132 offset:2048
	ds_read_b128 v[146:149], v132 offset:3072
	ds_read_b128 v[150:153], v133
	ds_read_b128 v[154:157], v133 offset:1024
	ds_read_b128 v[158:161], v133 offset:2048
	ds_read_b128 v[162:165], v133 offset:3072
	s_add_u32 s40, s40, 0x40000
	s_addc_u32 s41, s41, 0
	s_mov_b32 m0, s45
	v_lshl_add_u64 v[228:229], s[40:41], 0, v[194:195]
	ds_read_b128 v[166:169], v223 offset:32768
	ds_read_b128 v[178:181], v223 offset:33792
	ds_read_b128 v[182:185], v223 offset:34816
	ds_read_b128 v[200:203], v223 offset:35840
	ds_read_b128 v[204:207], v223 offset:36864
	ds_read_b128 v[208:211], v223 offset:37888
	ds_read_b128 v[212:215], v223 offset:38912
	ds_read_b128 v[216:219], v223 offset:39936
	global_load_lds_dwordx4 v[228:229], off
	v_lshl_add_u64 v[228:229], s[40:41], 0, v[192:193]
	s_mov_b32 m0, s46
	s_nop 0
	global_load_lds_dwordx4 v[228:229], off
	s_waitcnt vmcnt(8)
	s_waitcnt lgkmcnt(0)
	s_barrier
	v_mfma_f32_16x16x32_bf16 v[128:131], v[134:137], v[166:169], v[128:131]
	s_setprio 1
	v_mfma_f32_16x16x32_bf16 v[124:127], v[142:145], v[166:169], v[124:127]
	v_mfma_f32_16x16x32_bf16 v[116:119], v[142:145], v[182:185], v[116:119]
	v_mfma_f32_16x16x32_bf16 v[120:123], v[134:137], v[182:185], v[120:123]
	v_mfma_f32_16x16x32_bf16 v[112:115], v[134:137], v[204:207], v[112:115]
	v_mfma_f32_16x16x32_bf16 v[108:111], v[142:145], v[204:207], v[108:111]
	v_mfma_f32_16x16x32_bf16 v[100:103], v[142:145], v[212:215], v[100:103]
	v_mfma_f32_16x16x32_bf16 v[104:107], v[134:137], v[212:215], v[104:107]
	v_mfma_f32_16x16x32_bf16 v[128:131], v[138:141], v[178:181], v[128:131]
	v_mfma_f32_16x16x32_bf16 v[124:127], v[146:149], v[178:181], v[124:127]
	v_mfma_f32_16x16x32_bf16 v[116:119], v[146:149], v[200:203], v[116:119]
	v_mfma_f32_16x16x32_bf16 v[120:123], v[138:141], v[200:203], v[120:123]
	v_mfma_f32_16x16x32_bf16 v[112:115], v[138:141], v[208:211], v[112:115]
	v_mfma_f32_16x16x32_bf16 v[108:111], v[146:149], v[208:211], v[108:111]
	v_mfma_f32_16x16x32_bf16 v[100:103], v[146:149], v[216:219], v[100:103]
	v_mfma_f32_16x16x32_bf16 v[104:107], v[138:141], v[216:219], v[104:107]
	s_setprio 0
	s_setprio 1
	v_mfma_f32_16x16x32_bf16 v[96:99], v[150:153], v[166:169], v[96:99]
	v_mfma_f32_16x16x32_bf16 v[92:95], v[158:161], v[166:169], v[92:95]
	v_mfma_f32_16x16x32_bf16 v[84:87], v[158:161], v[182:185], v[84:87]
	v_mfma_f32_16x16x32_bf16 v[88:91], v[150:153], v[182:185], v[88:91]
	v_mfma_f32_16x16x32_bf16 v[80:83], v[150:153], v[204:207], v[80:83]
	v_mfma_f32_16x16x32_bf16 v[76:79], v[158:161], v[204:207], v[76:79]
	v_mfma_f32_16x16x32_bf16 v[68:71], v[158:161], v[212:215], v[68:71]
	v_mfma_f32_16x16x32_bf16 v[72:75], v[150:153], v[212:215], v[72:75]
	v_mfma_f32_16x16x32_bf16 v[96:99], v[154:157], v[178:181], v[96:99]
	v_mfma_f32_16x16x32_bf16 v[92:95], v[162:165], v[178:181], v[92:95]
	v_mfma_f32_16x16x32_bf16 v[84:87], v[162:165], v[200:203], v[84:87]
	v_mfma_f32_16x16x32_bf16 v[88:91], v[154:157], v[200:203], v[88:91]
	v_mfma_f32_16x16x32_bf16 v[80:83], v[154:157], v[208:211], v[80:83]
	v_mfma_f32_16x16x32_bf16 v[76:79], v[162:165], v[208:211], v[76:79]
	s_barrier
	v_mfma_f32_16x16x32_bf16 v[68:71], v[162:165], v[216:219], v[68:71]
	v_mfma_f32_16x16x32_bf16 v[72:75], v[154:157], v[216:219], v[72:75]
	s_setprio 0
	s_mov_b32 m0, s68
	v_lshl_add_u64 v[170:171], v[170:171], 0, s[18:19]
	s_add_u32 s30, s30, 0x40080
	ds_read_b128 v[166:169], v223 offset:49152
	ds_read_b128 v[178:181], v223 offset:50176
	ds_read_b128 v[182:185], v223 offset:51200
	ds_read_b128 v[200:203], v223 offset:52224
	ds_read_b128 v[204:207], v223 offset:53248
	ds_read_b128 v[208:211], v223 offset:54272
	ds_read_b128 v[212:215], v223 offset:55296
	ds_read_b128 v[216:219], v223 offset:56320
	global_load_lds_dwordx4 v[170:171], off
	v_lshl_add_u64 v[170:171], v[174:175], 0, s[18:19]
	s_mov_b32 m0, s69
	s_addc_u32 s31, s31, 0
	global_load_lds_dwordx4 v[170:171], off
	v_lshl_add_u64 v[170:171], s[30:31], 0, v[34:35]
	s_mov_b32 m0, s70
	s_nop 0
	global_load_lds_dwordx4 v[170:171], off
	v_lshl_add_u64 v[170:171], s[30:31], 0, v[190:191]
	s_mov_b32 m0, s71
	s_nop 0
	global_load_lds_dwordx4 v[170:171], off
	v_lshl_add_u64 v[170:171], v[224:225], 0, s[18:19]
	s_mov_b32 m0, s51
	s_nop 0
	global_load_lds_dwordx4 v[170:171], off
	v_lshl_add_u64 v[170:171], v[226:227], 0, s[18:19]
	s_mov_b32 m0, s52
	s_nop 0
	global_load_lds_dwordx4 v[170:171], off
	s_waitcnt vmcnt(8)
	s_waitcnt lgkmcnt(0)
	s_barrier
	v_mfma_f32_16x16x32_bf16 v[64:67], v[134:137], v[166:169], v[64:67]
	s_setprio 1
	v_mfma_f32_16x16x32_bf16 v[60:63], v[142:145], v[166:169], v[60:63]
	v_mfma_f32_16x16x32_bf16 v[52:55], v[142:145], v[182:185], v[52:55]
	v_mfma_f32_16x16x32_bf16 v[56:59], v[134:137], v[182:185], v[56:59]
	v_mfma_f32_16x16x32_bf16 v[48:51], v[134:137], v[204:207], v[48:51]
	v_mfma_f32_16x16x32_bf16 v[44:47], v[142:145], v[204:207], v[44:47]
	v_mfma_f32_16x16x32_bf16 v[36:39], v[142:145], v[212:215], v[36:39]
	v_mfma_f32_16x16x32_bf16 v[40:43], v[134:137], v[212:215], v[40:43]
	v_mfma_f32_16x16x32_bf16 v[64:67], v[138:141], v[178:181], v[64:67]
	v_mfma_f32_16x16x32_bf16 v[60:63], v[146:149], v[178:181], v[60:63]
	v_mfma_f32_16x16x32_bf16 v[52:55], v[146:149], v[200:203], v[52:55]
	v_mfma_f32_16x16x32_bf16 v[56:59], v[138:141], v[200:203], v[56:59]
	v_mfma_f32_16x16x32_bf16 v[48:51], v[138:141], v[208:211], v[48:51]
	v_mfma_f32_16x16x32_bf16 v[44:47], v[146:149], v[208:211], v[44:47]
	v_mfma_f32_16x16x32_bf16 v[36:39], v[146:149], v[216:219], v[36:39]
	v_mfma_f32_16x16x32_bf16 v[40:43], v[138:141], v[216:219], v[40:43]
	s_setprio 0
	s_setprio 1
	v_mfma_f32_16x16x32_bf16 v[30:33], v[150:153], v[166:169], v[30:33]
	v_mfma_f32_16x16x32_bf16 v[26:29], v[158:161], v[166:169], v[26:29]
	v_mfma_f32_16x16x32_bf16 v[18:21], v[158:161], v[182:185], v[18:21]
	v_mfma_f32_16x16x32_bf16 v[22:25], v[150:153], v[182:185], v[22:25]
	v_mfma_f32_16x16x32_bf16 v[14:17], v[150:153], v[204:207], v[14:17]
	v_mfma_f32_16x16x32_bf16 v[10:13], v[158:161], v[204:207], v[10:13]
	v_mfma_f32_16x16x32_bf16 v[2:5], v[158:161], v[212:215], v[2:5]
	v_mfma_f32_16x16x32_bf16 v[6:9], v[150:153], v[212:215], v[6:9]
	v_mfma_f32_16x16x32_bf16 v[30:33], v[154:157], v[178:181], v[30:33]
	v_mfma_f32_16x16x32_bf16 v[26:29], v[162:165], v[178:181], v[26:29]
	v_mfma_f32_16x16x32_bf16 v[18:21], v[162:165], v[200:203], v[18:21]
	v_mfma_f32_16x16x32_bf16 v[22:25], v[154:157], v[200:203], v[22:25]
	v_mfma_f32_16x16x32_bf16 v[14:17], v[154:157], v[208:211], v[14:17]
	v_mfma_f32_16x16x32_bf16 v[10:13], v[162:165], v[208:211], v[10:13]
	s_barrier
	v_mfma_f32_16x16x32_bf16 v[2:5], v[162:165], v[216:219], v[2:5]
	v_mfma_f32_16x16x32_bf16 v[6:9], v[154:157], v[216:219], v[6:9]
	s_setprio 0
	s_add_i32 s74, s74, 2
	s_add_u32 s36, s36, 0x100
	s_addc_u32 s37, s37, 0
	s_add_u32 s72, s72, 0x100
	s_addc_u32 s73, s73, 0
	s_cmp_gt_u32 s74, 13
	s_cbranch_scc0 .LBB0_541
	v_readlane_b32 s74, v255, 3
	s_and_b64 vcc, exec, s[10:11]
	v_readlane_b32 s75, v255, 4
	s_mov_b32 s58, 0x19b00000
	v_readlane_b32 s59, v255, 10
	s_mov_b32 s60, 0xff61b1e6
	s_mov_b64 s[62:63], 0x800
	s_mov_b32 s64, 0x3b000000
	s_cbranch_vccz .LBB0_544
	s_barrier
